# baseline (speedup 1.0000x reference)
.LBB1_5:
	v_add_u32_e32 v126, s5, v240
	ds_read_b64_tr_b16 v[122:123], v126 offset:24576
	ds_read_b64_tr_b16 v[124:125], v126 offset:25600
	s_waitcnt lgkmcnt(9)
	v_mfma_f32_32x32x16_f16 v[98:113], v[206:209], v[146:149], v[2:17]
	v_add_f32_e32 v82, v66, v67
	v_mov_b32_e32 v251, v68
	v_add_f32_e32 v82, v69, v82
	v_add_f32_e32 v251, v70, v251
	v_add_f32_e32 v82, v71, v82
	v_cvt_pk_f16_f32 v162, v66, v67
	v_cvt_pk_f16_f32 v163, v68, v69
	v_add_u32_e32 v128, s5, v239
	ds_read_b64_tr_b16 v[118:119], v128 offset:24576
	ds_read_b64_tr_b16 v[120:121], v128 offset:25600
	v_add_f32_e32 v66, v72, v82
	s_waitcnt lgkmcnt(10)
	v_mfma_f32_32x32x16_f16 v[82:97], v[202:205], v[146:149], v[2:17]
	v_add_f32_e32 v251, v73, v251
	v_add_f32_e32 v66, v74, v66
	v_add_f32_e32 v251, v75, v251
	v_cvt_pk_f16_f32 v164, v70, v71
	v_cvt_pk_f16_f32 v165, v72, v73
	ds_read_b64_tr_b16 v[114:115], v126 offset:26624
	ds_read_b64_tr_b16 v[116:117], v126 offset:27648
	s_waitcnt lgkmcnt(11)
	v_mfma_f32_32x32x16_f16 v[98:113], v[198:201], v[150:153], v[98:113]
	v_add_f32_e32 v66, v76, v66
	v_add_f32_e32 v251, v77, v251
	v_add_f32_e32 v66, v78, v66
	v_add_f32_e32 v251, v79, v251
	v_cvt_pk_f16_f32 v166, v74, v75
	v_cvt_pk_f16_f32 v167, v76, v77
	ds_read_b64_tr_b16 v[70:71], v128 offset:26624
	ds_read_b64_tr_b16 v[72:73], v128 offset:27648
	s_waitcnt lgkmcnt(12)
	v_mfma_f32_32x32x16_f16 v[82:97], v[194:197], v[150:153], v[82:97]
	v_add_f32_e32 v66, v80, v66
	v_add_f32_e32 v251, v81, v251
	v_add_f32_e32 v66, v50, v66
	v_add_f32_e32 v74, v51, v66
	v_cvt_pk_f16_f32 v168, v78, v79
	v_cvt_pk_f16_f32 v169, v80, v81
	ds_read_b64_tr_b16 v[66:67], v126 offset:28672
	ds_read_b64_tr_b16 v[68:69], v126 offset:29696
	s_waitcnt lgkmcnt(13)
	v_mfma_f32_32x32x16_f16 v[98:113], v[190:193], v[154:157], v[98:113]
	v_add_f32_e32 v251, v52, v251
	v_add_f32_e32 v74, v53, v74
	v_add_f32_e32 v251, v54, v251
	v_add_f32_e32 v74, v55, v74
	v_cvt_pk_f16_f32 v170, v50, v51
	v_cvt_pk_f16_f32 v171, v52, v53
	ds_read_b64_tr_b16 v[50:51], v128 offset:28672
	ds_read_b64_tr_b16 v[52:53], v128 offset:29696
	s_waitcnt lgkmcnt(14)
	v_mfma_f32_32x32x16_f16 v[82:97], v[186:189], v[154:157], v[82:97]
	v_add_f32_e32 v251, v56, v251
	v_add_f32_e32 v74, v57, v74
	v_add_f32_e32 v251, v58, v251
	v_add_f32_e32 v74, v59, v74
	v_cvt_pk_f16_f32 v172, v54, v55
	v_cvt_pk_f16_f32 v173, v56, v57
	ds_read_b64_tr_b16 v[54:55], v126 offset:30720
	ds_read_b64_tr_b16 v[56:57], v126 offset:31744
	s_waitcnt lgkmcnt(14)
	v_mfma_f32_32x32x16_f16 v[98:113], v[182:185], v[158:161], v[98:113]
	v_add_f32_e32 v251, v60, v251
	v_add_f32_e32 v74, v61, v74
	v_add_f32_e32 v251, v62, v251
	v_add_f32_e32 v74, v63, v74
	v_cvt_pk_f16_f32 v174, v58, v59
	v_cvt_pk_f16_f32 v175, v60, v61
	ds_read_b64_tr_b16 v[58:59], v128 offset:30720
	ds_read_b64_tr_b16 v[60:61], v128 offset:31744
	v_mfma_f32_32x32x16_f16 v[82:97], v[178:181], v[158:161], v[82:97]
	v_add_f32_e32 v251, v64, v251
	v_add_f32_e32 v74, v65, v74
	v_add_f32_e32 v74, v251, v74
	v_cvt_pk_f16_f32 v176, v62, v63
	v_cvt_pk_f16_f32 v177, v64, v65
	v_max_f32_e32 v62, v99, v98
	v_max3_f32 v63, v100, v101, v102
	v_max3_f32 v62, v62, v103, v104
	v_max3_f32 v63, v63, v105, v106
	v_max3_f32 v62, v62, v107, v108
	v_max3_f32 v63, v63, v109, v110
	v_max3_f32 v62, v62, v111, v112
	v_max3_f32 v63, v63, v113, v82
	v_max3_f32 v62, v62, v83, v84
	v_max3_f32 v63, v63, v85, v86
	v_max3_f32 v62, v62, v87, v88
	v_max3_f32 v63, v63, v89, v90
	v_max3_f32 v62, v62, v91, v92
	v_max3_f32 v63, v63, v93, v94
	v_max3_f32 v62, v62, v95, v96
	v_max3_f32 v62, v62, v97, v63
	v_mov_b32_e32 v63, v62
	s_nop 1
	v_permlane32_swap_b32_e32 v62, v63
	v_max_f32_e32 v62, v63, v62
	v_cmp_lt_f32_e32 vcc, s34, v62
	s_cmp_lg_u64 vcc, 0
	v_add_f32_e32 v182, v127, v74
	s_cselect_b64 s[8:9], -1, 0
	s_cbranch_vccnz .LBB1_25

.LBB1_12:
	v_add_u32_e32 v174, s35, v240
	ds_read_b64_tr_b16 v[134:135], v174 offset:24576
	ds_read_b64_tr_b16 v[136:137], v174 offset:25600
	s_waitcnt lgkmcnt(9)
	v_mfma_f32_32x32x16_f16 v[66:81], v[62:65], v[146:149], v[2:17]
	v_add_f32_e32 v50, v98, v99
	v_mov_b32_e32 v251, v100
	v_add_f32_e32 v50, v101, v50
	v_add_f32_e32 v251, v102, v251
	v_add_f32_e32 v50, v103, v50
	v_cvt_pk_f16_f32 v162, v98, v99
	v_cvt_pk_f16_f32 v163, v100, v101
	v_add_u32_e32 v183, s35, v239
	ds_read_b64_tr_b16 v[142:143], v183 offset:24576
	ds_read_b64_tr_b16 v[144:145], v183 offset:25600
	v_add_f32_e32 v251, v104, v251
	v_add_f32_e32 v50, v105, v50
	v_add_f32_e32 v251, v106, v251
	v_add_f32_e32 v98, v107, v50
	s_waitcnt lgkmcnt(10)
	v_mfma_f32_32x32x16_f16 v[50:65], v[138:141], v[146:149], v[2:17]
	v_cvt_pk_f16_f32 v164, v102, v103
	v_cvt_pk_f16_f32 v165, v104, v105
	ds_read_b64_tr_b16 v[138:139], v174 offset:26624
	ds_read_b64_tr_b16 v[140:141], v174 offset:27648
	s_waitcnt lgkmcnt(11)
	v_mfma_f32_32x32x16_f16 v[66:81], v[178:181], v[150:153], v[66:81]
	v_add_f32_e32 v251, v108, v251
	v_add_f32_e32 v98, v109, v98
	v_add_f32_e32 v251, v110, v251
	v_add_f32_e32 v98, v111, v98
	v_cvt_pk_f16_f32 v166, v106, v107
	v_cvt_pk_f16_f32 v167, v108, v109
	ds_read_b64_tr_b16 v[102:103], v183 offset:26624
	ds_read_b64_tr_b16 v[104:105], v183 offset:27648
	s_waitcnt lgkmcnt(12)
	v_mfma_f32_32x32x16_f16 v[50:65], v[126:129], v[150:153], v[50:65]
	v_add_f32_e32 v251, v112, v251
	v_add_f32_e32 v98, v113, v98
	v_add_f32_e32 v251, v82, v251
	v_add_f32_e32 v106, v83, v98
	v_cvt_pk_f16_f32 v168, v110, v111
	v_cvt_pk_f16_f32 v169, v112, v113
	ds_read_b64_tr_b16 v[98:99], v174 offset:28672
	ds_read_b64_tr_b16 v[100:101], v174 offset:29696
	s_waitcnt lgkmcnt(13)
	v_mfma_f32_32x32x16_f16 v[66:81], v[130:133], v[154:157], v[66:81]
	v_add_f32_e32 v251, v84, v251
	v_add_f32_e32 v106, v85, v106
	v_add_f32_e32 v251, v86, v251
	v_add_f32_e32 v106, v87, v106
	v_cvt_pk_f16_f32 v170, v82, v83
	v_cvt_pk_f16_f32 v171, v84, v85
	ds_read_b64_tr_b16 v[82:83], v183 offset:28672
	ds_read_b64_tr_b16 v[84:85], v183 offset:29696
	s_waitcnt lgkmcnt(14)
	v_mfma_f32_32x32x16_f16 v[50:65], v[118:121], v[154:157], v[50:65]
	v_add_f32_e32 v251, v88, v251
	v_add_f32_e32 v106, v89, v106
	v_add_f32_e32 v251, v90, v251
	v_add_f32_e32 v106, v91, v106
	v_cvt_pk_f16_f32 v172, v86, v87
	v_cvt_pk_f16_f32 v173, v88, v89
	ds_read_b64_tr_b16 v[86:87], v174 offset:30720
	ds_read_b64_tr_b16 v[88:89], v174 offset:31744
	s_waitcnt lgkmcnt(14)
	v_mfma_f32_32x32x16_f16 v[66:81], v[122:125], v[158:161], v[66:81]
	v_add_f32_e32 v251, v92, v251
	v_add_f32_e32 v106, v93, v106
	v_add_f32_e32 v251, v94, v251
	v_add_f32_e32 v106, v95, v106
	v_cvt_pk_f16_f32 v174, v90, v91
	v_cvt_pk_f16_f32 v175, v92, v93
	ds_read_b64_tr_b16 v[90:91], v183 offset:30720
	ds_read_b64_tr_b16 v[92:93], v183 offset:31744
	v_mfma_f32_32x32x16_f16 v[50:65], v[114:117], v[158:161], v[50:65]
	v_add_f32_e32 v251, v96, v251
	v_add_f32_e32 v106, v97, v106
	v_add_f32_e32 v106, v251, v106
	v_cvt_pk_f16_f32 v176, v94, v95
	v_cvt_pk_f16_f32 v177, v96, v97
	v_max_f32_e32 v94, v67, v66
	v_max3_f32 v95, v68, v69, v70
	v_max3_f32 v94, v94, v71, v72
	v_max3_f32 v95, v95, v73, v74
	v_max3_f32 v94, v94, v75, v76
	v_max3_f32 v95, v95, v77, v78
	v_max3_f32 v94, v94, v79, v80
	v_max3_f32 v95, v95, v81, v50
	v_max3_f32 v94, v94, v51, v52
	v_max3_f32 v95, v95, v53, v54
	v_max3_f32 v94, v94, v55, v56
	v_max3_f32 v95, v95, v57, v58
	v_max3_f32 v94, v94, v59, v60
	v_max3_f32 v95, v95, v61, v62
	v_max3_f32 v94, v94, v63, v64
	v_max3_f32 v94, v94, v65, v95
	v_mov_b32_e32 v95, v94
	s_nop 1
	v_permlane32_swap_b32_e32 v94, v95
	v_max_f32_e32 v94, v95, v94
	v_cmp_lt_f32_e32 vcc, s34, v94
	s_cmp_lg_u64 vcc, 0
	v_add_f32_e32 v127, v182, v106
	s_cselect_b64 s[8:9], -1, 0
	s_cbranch_vccnz .LBB1_28
